# MoE up-projection epilogue: packed f32 math + permlane16_swap pairing for 16-byte stores (4 dwordx4 instead of 8 dwordx2), plus MLA loop changes
# baseline (speedup 1.0000x reference)
; __device__ __forceinline__ u32x4 pack8(const f32x4 a, const f32x4 b) { u32x4 w; w.x = cvt_pk_bf16(a[0], a[1]); w.y = cvt_pk_bf16(a[2], a[3]); w.z = cvt_pk_bf16(b[0], b[1]); w.w = cvt_pk_bf16(b[2], b[3]); return w; }
; __device__ __forceinline__ float silu_f(float x) { return x * __builtin_amdgcn_rcpf(1.0f + __builtin_amdgcn_exp2f(-1.4426950409f * x)); }
;     w = __builtin_amdgcn_cvt_pk_fp8_f32(__builtin_amdgcn_fmed3f(v[2] * 8.0f, -448.0f, 448.0f), __builtin_amdgcn_fmed3f(v[3] * 8.0f, -448.0f, 448.0f), w, true); return (unsigned)w; }
;     __device__ __forceinline__ void operator()(const f32x4 (&acc)[2][2][4][2], const Unit& u, int wr, int wc, int fr, int fq) const {
;     ...
;         for (int ai = 0; ai < 2; ++ai)
; #pragma unroll
;             for (int m = 0; m < 4; ++m) {
;                 const float r = rs[ai][m]; f32x4 o[2];
; #pragma unroll
;                 for (int n = 0; n < 2; ++n) { const f32x4 a = acc[ai][0][m][n] * r, b = acc[ai][1][m][n] * r;
;                     o[n] = (f32x4){silu_f(a[0]) * b[0], silu_f(a[1]) * b[1], silu_f(a[2]) * b[2], silu_f(a[3]) * b[3]}; }
;                 if (F8OUT) { u32x2 w; w.x = pack4_fp8(o[0]); w.y = pack4_fp8(o[1]); *(u32x2*)((unsigned char*)h + (size_t)(row0 + ai * HALF + m * 16) * FFN + col0) = w; }
;                 else *(u32x4*)(h + (size_t)(row0 + ai * HALF + m * 16) * FFN + col0) = pack8(o[0], o[1]);
.LBB0_1375:
	v_mov_b32_e32 v22, 0xbfb8aa3b
	v_mov_b32_e32 v24, 0x41000000
	v_mov_b32_e32 v26, 1.0
	v_pk_mul_f32 v[4:5], v[154:155], v[22:23] op_sel_hi:[1,0]
	v_pk_mul_f32 v[6:7], v[156:157], v[22:23] op_sel_hi:[1,0]
	v_pk_mul_f32 v[8:9], v[150:151], v[22:23] op_sel_hi:[1,0]
	v_pk_mul_f32 v[10:11], v[152:153], v[22:23] op_sel_hi:[1,0]
	v_exp_f32_e32 v4, v4
	v_exp_f32_e32 v5, v5
	v_exp_f32_e32 v6, v6
	v_exp_f32_e32 v7, v7
	v_exp_f32_e32 v8, v8
	v_exp_f32_e32 v9, v9
	v_exp_f32_e32 v10, v10
	v_exp_f32_e32 v11, v11
	v_pk_add_f32 v[4:5], v[4:5], v[26:27] op_sel_hi:[1,0]
	v_pk_add_f32 v[6:7], v[6:7], v[26:27] op_sel_hi:[1,0]
	v_pk_add_f32 v[8:9], v[8:9], v[26:27] op_sel_hi:[1,0]
	v_pk_add_f32 v[10:11], v[10:11], v[26:27] op_sel_hi:[1,0]
	v_rcp_f32_e32 v4, v4
	v_rcp_f32_e32 v5, v5
	v_rcp_f32_e32 v6, v6
	v_rcp_f32_e32 v7, v7
	v_rcp_f32_e32 v8, v8
	v_rcp_f32_e32 v9, v9
	v_rcp_f32_e32 v10, v10
	v_rcp_f32_e32 v11, v11
	v_pk_mul_f32 v[4:5], v[154:155], v[4:5]
	v_pk_mul_f32 v[6:7], v[156:157], v[6:7]
	v_pk_mul_f32 v[8:9], v[150:151], v[8:9]
	v_pk_mul_f32 v[10:11], v[152:153], v[10:11]
	v_pk_mul_f32 v[4:5], v[158:159], v[4:5]
	v_pk_mul_f32 v[6:7], v[160:161], v[6:7]
	v_pk_mul_f32 v[8:9], v[146:147], v[8:9]
	v_pk_mul_f32 v[10:11], v[148:149], v[10:11]
	v_pk_mul_f32 v[4:5], v[4:5], v[24:25] op_sel_hi:[1,0]
	v_pk_mul_f32 v[6:7], v[6:7], v[24:25] op_sel_hi:[1,0]
	v_pk_mul_f32 v[8:9], v[8:9], v[24:25] op_sel_hi:[1,0]
	v_pk_mul_f32 v[10:11], v[10:11], v[24:25] op_sel_hi:[1,0]
	v_med3_f32 v4, v4, s64, v250
	v_med3_f32 v5, v5, s64, v250
	v_med3_f32 v6, v6, s64, v250
	v_med3_f32 v7, v7, s64, v250
	v_med3_f32 v8, v8, s64, v250
	v_med3_f32 v9, v9, s64, v250
	v_med3_f32 v10, v10, s64, v250
	v_med3_f32 v11, v11, s64, v250
	v_cvt_pk_fp8_f32 v12, v4, v5
	v_cvt_pk_fp8_f32 v13, v8, v9
	s_nop 0
	v_cvt_pk_fp8_f32 v12, v6, v7 op_sel:[0,0,1]
	v_cvt_pk_fp8_f32 v13, v10, v11 op_sel:[0,0,1]
	v_pk_mul_f32 v[4:5], v[142:143], v[22:23] op_sel_hi:[1,0]
	v_pk_mul_f32 v[6:7], v[144:145], v[22:23] op_sel_hi:[1,0]
	v_pk_mul_f32 v[8:9], v[134:135], v[22:23] op_sel_hi:[1,0]
	v_pk_mul_f32 v[10:11], v[136:137], v[22:23] op_sel_hi:[1,0]
	v_exp_f32_e32 v4, v4
	v_exp_f32_e32 v5, v5
	v_exp_f32_e32 v6, v6
	v_exp_f32_e32 v7, v7
	v_exp_f32_e32 v8, v8
	v_exp_f32_e32 v9, v9
	v_exp_f32_e32 v10, v10
	v_exp_f32_e32 v11, v11
	v_pk_add_f32 v[4:5], v[4:5], v[26:27] op_sel_hi:[1,0]
	v_pk_add_f32 v[6:7], v[6:7], v[26:27] op_sel_hi:[1,0]
	v_pk_add_f32 v[8:9], v[8:9], v[26:27] op_sel_hi:[1,0]
	v_pk_add_f32 v[10:11], v[10:11], v[26:27] op_sel_hi:[1,0]
	v_rcp_f32_e32 v4, v4
	v_rcp_f32_e32 v5, v5
	v_rcp_f32_e32 v6, v6
	v_rcp_f32_e32 v7, v7
	v_rcp_f32_e32 v8, v8
	v_rcp_f32_e32 v9, v9
	v_rcp_f32_e32 v10, v10
	v_rcp_f32_e32 v11, v11
	v_pk_mul_f32 v[4:5], v[142:143], v[4:5]
	v_pk_mul_f32 v[6:7], v[144:145], v[6:7]
	v_pk_mul_f32 v[8:9], v[134:135], v[8:9]
	v_pk_mul_f32 v[10:11], v[136:137], v[10:11]
	v_pk_mul_f32 v[4:5], v[138:139], v[4:5]
	v_pk_mul_f32 v[6:7], v[140:141], v[6:7]
	v_pk_mul_f32 v[8:9], v[130:131], v[8:9]
	v_pk_mul_f32 v[10:11], v[132:133], v[10:11]
	v_pk_mul_f32 v[4:5], v[4:5], v[24:25] op_sel_hi:[1,0]
	v_pk_mul_f32 v[6:7], v[6:7], v[24:25] op_sel_hi:[1,0]
	v_pk_mul_f32 v[8:9], v[8:9], v[24:25] op_sel_hi:[1,0]
	v_pk_mul_f32 v[10:11], v[10:11], v[24:25] op_sel_hi:[1,0]
	v_med3_f32 v4, v4, s64, v250
	v_med3_f32 v5, v5, s64, v250
	v_med3_f32 v6, v6, s64, v250
	v_med3_f32 v7, v7, s64, v250
	v_med3_f32 v8, v8, s64, v250
	v_med3_f32 v9, v9, s64, v250
	v_med3_f32 v10, v10, s64, v250
	v_med3_f32 v11, v11, s64, v250
	v_cvt_pk_fp8_f32 v14, v4, v5
	v_cvt_pk_fp8_f32 v15, v8, v9
	s_nop 0
	v_cvt_pk_fp8_f32 v14, v6, v7 op_sel:[0,0,1]
	v_cvt_pk_fp8_f32 v15, v10, v11 op_sel:[0,0,1]
	v_lshl_or_b32 v2, s62, 7, v193
	v_ashrrev_i32_e32 v3, 31, v2
	v_lshl_add_u32 v0, s63, 8, v163
	v_lshl_add_u64 v[2:3], s[20:21], 0, v[2:3]
	v_mbcnt_lo_u32_b32 v20, -1, 0
	v_mbcnt_hi_u32_b32 v20, -1, v20
	v_and_b32_e32 v20, 16, v20
	v_lshrrev_b32_e32 v21, 1, v20
	v_sub_co_u32_e32 v2, vcc, v2, v21
	s_nop 1
	v_subbrev_co_u32_e32 v3, vcc, 0, v3, vcc
	v_add_u32_e32 v0, v0, v20
	s_nop 15
	s_nop 15
	s_nop 1
	v_permlane16_swap_b32_e32 v12, v14
	v_permlane16_swap_b32_e32 v13, v15
	v_mad_i64_i32 v[18:19], s[22:23], v0, s73, v[2:3]
	s_waitcnt vmcnt(0)
	global_store_dwordx4 v[18:19], v[12:15], off
	v_pk_mul_f32 v[4:5], v[126:127], v[22:23] op_sel_hi:[1,0]
	v_pk_mul_f32 v[6:7], v[128:129], v[22:23] op_sel_hi:[1,0]
	v_pk_mul_f32 v[8:9], v[118:119], v[22:23] op_sel_hi:[1,0]
	v_pk_mul_f32 v[10:11], v[120:121], v[22:23] op_sel_hi:[1,0]
	v_exp_f32_e32 v4, v4
	v_exp_f32_e32 v5, v5
	v_exp_f32_e32 v6, v6
	v_exp_f32_e32 v7, v7
	v_exp_f32_e32 v8, v8
	v_exp_f32_e32 v9, v9
	v_exp_f32_e32 v10, v10
	v_exp_f32_e32 v11, v11
	v_pk_add_f32 v[4:5], v[4:5], v[26:27] op_sel_hi:[1,0]
	v_pk_add_f32 v[6:7], v[6:7], v[26:27] op_sel_hi:[1,0]
	v_pk_add_f32 v[8:9], v[8:9], v[26:27] op_sel_hi:[1,0]
	v_pk_add_f32 v[10:11], v[10:11], v[26:27] op_sel_hi:[1,0]
	v_rcp_f32_e32 v4, v4
	v_rcp_f32_e32 v5, v5
	v_rcp_f32_e32 v6, v6
	v_rcp_f32_e32 v7, v7
	v_rcp_f32_e32 v8, v8
	v_rcp_f32_e32 v9, v9
	v_rcp_f32_e32 v10, v10
	v_rcp_f32_e32 v11, v11
	v_pk_mul_f32 v[4:5], v[126:127], v[4:5]
	v_pk_mul_f32 v[6:7], v[128:129], v[6:7]
	v_pk_mul_f32 v[8:9], v[118:119], v[8:9]
	v_pk_mul_f32 v[10:11], v[120:121], v[10:11]
	v_pk_mul_f32 v[4:5], v[122:123], v[4:5]
	v_pk_mul_f32 v[6:7], v[124:125], v[6:7]
	v_pk_mul_f32 v[8:9], v[114:115], v[8:9]
	v_pk_mul_f32 v[10:11], v[116:117], v[10:11]
	v_pk_mul_f32 v[4:5], v[4:5], v[24:25] op_sel_hi:[1,0]
	v_pk_mul_f32 v[6:7], v[6:7], v[24:25] op_sel_hi:[1,0]
	v_pk_mul_f32 v[8:9], v[8:9], v[24:25] op_sel_hi:[1,0]
	v_pk_mul_f32 v[10:11], v[10:11], v[24:25] op_sel_hi:[1,0]
; __device__ __forceinline__ u32x4 pack8(const f32x4 a, const f32x4 b) { u32x4 w; w.x = cvt_pk_bf16(a[0], a[1]); w.y = cvt_pk_bf16(a[2], a[3]); w.z = cvt_pk_bf16(b[0], b[1]); w.w = cvt_pk_bf16(b[2], b[3]); return w; }
; __device__ __forceinline__ float silu_f(float x) { return x * __builtin_amdgcn_rcpf(1.0f + __builtin_amdgcn_exp2f(-1.4426950409f * x)); }
;     w = __builtin_amdgcn_cvt_pk_fp8_f32(__builtin_amdgcn_fmed3f(v[2] * 8.0f, -448.0f, 448.0f), __builtin_amdgcn_fmed3f(v[3] * 8.0f, -448.0f, 448.0f), w, true); return (unsigned)w; }
;     __device__ __forceinline__ void operator()(const f32x4 (&acc)[2][2][4][2], const Unit& u, int wr, int wc, int fr, int fq) const {
;     ...
;         for (int ai = 0; ai < 2; ++ai)
; #pragma unroll
;             for (int m = 0; m < 4; ++m) {
;                 const float r = rs[ai][m]; f32x4 o[2];
; #pragma unroll
;                 for (int n = 0; n < 2; ++n) { const f32x4 a = acc[ai][0][m][n] * r, b = acc[ai][1][m][n] * r;
;                     o[n] = (f32x4){silu_f(a[0]) * b[0], silu_f(a[1]) * b[1], silu_f(a[2]) * b[2], silu_f(a[3]) * b[3]}; }
;                 if (F8OUT) { u32x2 w; w.x = pack4_fp8(o[0]); w.y = pack4_fp8(o[1]); *(u32x2*)((unsigned char*)h + (size_t)(row0 + ai * HALF + m * 16) * FFN + col0) = w; }
;                 else *(u32x4*)(h + (size_t)(row0 + ai * HALF + m * 16) * FFN + col0) = pack8(o[0], o[1]);
	v_med3_f32 v4, v4, s64, v250
	v_med3_f32 v5, v5, s64, v250
	v_med3_f32 v6, v6, s64, v250
	v_med3_f32 v7, v7, s64, v250
	v_med3_f32 v8, v8, s64, v250
	v_med3_f32 v9, v9, s64, v250
	v_med3_f32 v10, v10, s64, v250
	v_med3_f32 v11, v11, s64, v250
	v_cvt_pk_fp8_f32 v12, v4, v5
	v_cvt_pk_fp8_f32 v13, v8, v9
	s_nop 0
	v_cvt_pk_fp8_f32 v12, v6, v7 op_sel:[0,0,1]
	v_cvt_pk_fp8_f32 v13, v10, v11 op_sel:[0,0,1]
	v_pk_mul_f32 v[4:5], v[110:111], v[22:23] op_sel_hi:[1,0]
	v_pk_mul_f32 v[6:7], v[112:113], v[22:23] op_sel_hi:[1,0]
	v_pk_mul_f32 v[8:9], v[102:103], v[22:23] op_sel_hi:[1,0]
	v_pk_mul_f32 v[10:11], v[104:105], v[22:23] op_sel_hi:[1,0]
	v_exp_f32_e32 v4, v4
	v_exp_f32_e32 v5, v5
	v_exp_f32_e32 v6, v6
	v_exp_f32_e32 v7, v7
	v_exp_f32_e32 v8, v8
	v_exp_f32_e32 v9, v9
	v_exp_f32_e32 v10, v10
	v_exp_f32_e32 v11, v11
	v_pk_add_f32 v[4:5], v[4:5], v[26:27] op_sel_hi:[1,0]
	v_pk_add_f32 v[6:7], v[6:7], v[26:27] op_sel_hi:[1,0]
	v_pk_add_f32 v[8:9], v[8:9], v[26:27] op_sel_hi:[1,0]
	v_pk_add_f32 v[10:11], v[10:11], v[26:27] op_sel_hi:[1,0]
	v_rcp_f32_e32 v4, v4
	v_rcp_f32_e32 v5, v5
	v_rcp_f32_e32 v6, v6
	v_rcp_f32_e32 v7, v7
	v_rcp_f32_e32 v8, v8
	v_rcp_f32_e32 v9, v9
	v_rcp_f32_e32 v10, v10
	v_rcp_f32_e32 v11, v11
	v_pk_mul_f32 v[4:5], v[110:111], v[4:5]
	v_pk_mul_f32 v[6:7], v[112:113], v[6:7]
	v_pk_mul_f32 v[8:9], v[102:103], v[8:9]
	v_pk_mul_f32 v[10:11], v[104:105], v[10:11]
	v_pk_mul_f32 v[4:5], v[106:107], v[4:5]
	v_pk_mul_f32 v[6:7], v[108:109], v[6:7]
	v_pk_mul_f32 v[8:9], v[98:99], v[8:9]
	v_pk_mul_f32 v[10:11], v[100:101], v[10:11]
	v_pk_mul_f32 v[4:5], v[4:5], v[24:25] op_sel_hi:[1,0]
	v_pk_mul_f32 v[6:7], v[6:7], v[24:25] op_sel_hi:[1,0]
	v_pk_mul_f32 v[8:9], v[8:9], v[24:25] op_sel_hi:[1,0]
	v_pk_mul_f32 v[10:11], v[10:11], v[24:25] op_sel_hi:[1,0]
	v_med3_f32 v4, v4, s64, v250
	v_med3_f32 v5, v5, s64, v250
	v_med3_f32 v6, v6, s64, v250
	v_med3_f32 v7, v7, s64, v250
	v_med3_f32 v8, v8, s64, v250
	v_med3_f32 v9, v9, s64, v250
	v_med3_f32 v10, v10, s64, v250
	v_med3_f32 v11, v11, s64, v250
	v_cvt_pk_fp8_f32 v14, v4, v5
	v_cvt_pk_fp8_f32 v15, v8, v9
	s_nop 0
	v_cvt_pk_fp8_f32 v14, v6, v7 op_sel:[0,0,1]
	v_cvt_pk_fp8_f32 v15, v10, v11 op_sel:[0,0,1]
	s_nop 1
	v_permlane16_swap_b32_e32 v12, v14
	v_permlane16_swap_b32_e32 v13, v15
	v_add_u32_e32 v18, 32, v0
	v_mad_i64_i32 v[18:19], s[22:23], v18, s73, v[2:3]
	global_store_dwordx4 v[18:19], v[12:15], off
	v_pk_mul_f32 v[4:5], v[94:95], v[22:23] op_sel_hi:[1,0]
	v_pk_mul_f32 v[6:7], v[96:97], v[22:23] op_sel_hi:[1,0]
	v_pk_mul_f32 v[8:9], v[86:87], v[22:23] op_sel_hi:[1,0]
	v_pk_mul_f32 v[10:11], v[88:89], v[22:23] op_sel_hi:[1,0]
	v_exp_f32_e32 v4, v4
	v_exp_f32_e32 v5, v5
	v_exp_f32_e32 v6, v6
	v_exp_f32_e32 v7, v7
	v_exp_f32_e32 v8, v8
	v_exp_f32_e32 v9, v9
	v_exp_f32_e32 v10, v10
	v_exp_f32_e32 v11, v11
	v_pk_add_f32 v[4:5], v[4:5], v[26:27] op_sel_hi:[1,0]
	v_pk_add_f32 v[6:7], v[6:7], v[26:27] op_sel_hi:[1,0]
	v_pk_add_f32 v[8:9], v[8:9], v[26:27] op_sel_hi:[1,0]
	v_pk_add_f32 v[10:11], v[10:11], v[26:27] op_sel_hi:[1,0]
	v_rcp_f32_e32 v4, v4
	v_rcp_f32_e32 v5, v5
	v_rcp_f32_e32 v6, v6
	v_rcp_f32_e32 v7, v7
	v_rcp_f32_e32 v8, v8
	v_rcp_f32_e32 v9, v9
	v_rcp_f32_e32 v10, v10
	v_rcp_f32_e32 v11, v11
	v_pk_mul_f32 v[4:5], v[94:95], v[4:5]
	v_pk_mul_f32 v[6:7], v[96:97], v[6:7]
	v_pk_mul_f32 v[8:9], v[86:87], v[8:9]
	v_pk_mul_f32 v[10:11], v[88:89], v[10:11]
	v_pk_mul_f32 v[4:5], v[90:91], v[4:5]
	v_pk_mul_f32 v[6:7], v[92:93], v[6:7]
	v_pk_mul_f32 v[8:9], v[82:83], v[8:9]
	v_pk_mul_f32 v[10:11], v[84:85], v[10:11]
	v_pk_mul_f32 v[4:5], v[4:5], v[24:25] op_sel_hi:[1,0]
	v_pk_mul_f32 v[6:7], v[6:7], v[24:25] op_sel_hi:[1,0]
	v_pk_mul_f32 v[8:9], v[8:9], v[24:25] op_sel_hi:[1,0]
	v_pk_mul_f32 v[10:11], v[10:11], v[24:25] op_sel_hi:[1,0]
	v_med3_f32 v4, v4, s64, v250
	v_med3_f32 v5, v5, s64, v250
	v_med3_f32 v6, v6, s64, v250
	v_med3_f32 v7, v7, s64, v250
	v_med3_f32 v8, v8, s64, v250
	v_med3_f32 v9, v9, s64, v250
	v_med3_f32 v10, v10, s64, v250
	v_med3_f32 v11, v11, s64, v250
	v_cvt_pk_fp8_f32 v12, v4, v5
	v_cvt_pk_fp8_f32 v13, v8, v9
	s_nop 0
	v_cvt_pk_fp8_f32 v12, v6, v7 op_sel:[0,0,1]
	v_cvt_pk_fp8_f32 v13, v10, v11 op_sel:[0,0,1]
	v_pk_mul_f32 v[4:5], v[78:79], v[22:23] op_sel_hi:[1,0]
	v_pk_mul_f32 v[6:7], v[80:81], v[22:23] op_sel_hi:[1,0]
	v_pk_mul_f32 v[8:9], v[70:71], v[22:23] op_sel_hi:[1,0]
	v_pk_mul_f32 v[10:11], v[72:73], v[22:23] op_sel_hi:[1,0]
	v_exp_f32_e32 v4, v4
	v_exp_f32_e32 v5, v5
	v_exp_f32_e32 v6, v6
	v_exp_f32_e32 v7, v7
	v_exp_f32_e32 v8, v8
	v_exp_f32_e32 v9, v9
	v_exp_f32_e32 v10, v10
	v_exp_f32_e32 v11, v11
	v_pk_add_f32 v[4:5], v[4:5], v[26:27] op_sel_hi:[1,0]
	v_pk_add_f32 v[6:7], v[6:7], v[26:27] op_sel_hi:[1,0]
	v_pk_add_f32 v[8:9], v[8:9], v[26:27] op_sel_hi:[1,0]
	v_pk_add_f32 v[10:11], v[10:11], v[26:27] op_sel_hi:[1,0]
	v_rcp_f32_e32 v4, v4
	v_rcp_f32_e32 v5, v5
	v_rcp_f32_e32 v6, v6
	v_rcp_f32_e32 v7, v7
	v_rcp_f32_e32 v8, v8
	v_rcp_f32_e32 v9, v9
	v_rcp_f32_e32 v10, v10
	v_rcp_f32_e32 v11, v11
	v_pk_mul_f32 v[4:5], v[78:79], v[4:5]
; __device__ __forceinline__ u32x4 pack8(const f32x4 a, const f32x4 b) { u32x4 w; w.x = cvt_pk_bf16(a[0], a[1]); w.y = cvt_pk_bf16(a[2], a[3]); w.z = cvt_pk_bf16(b[0], b[1]); w.w = cvt_pk_bf16(b[2], b[3]); return w; }
; __device__ __forceinline__ float silu_f(float x) { return x * __builtin_amdgcn_rcpf(1.0f + __builtin_amdgcn_exp2f(-1.4426950409f * x)); }
;     w = __builtin_amdgcn_cvt_pk_fp8_f32(__builtin_amdgcn_fmed3f(v[2] * 8.0f, -448.0f, 448.0f), __builtin_amdgcn_fmed3f(v[3] * 8.0f, -448.0f, 448.0f), w, true); return (unsigned)w; }
;     __device__ __forceinline__ void operator()(const f32x4 (&acc)[2][2][4][2], const Unit& u, int wr, int wc, int fr, int fq) const {
;     ...
;         for (int ai = 0; ai < 2; ++ai)
; #pragma unroll
;             for (int m = 0; m < 4; ++m) {
;                 const float r = rs[ai][m]; f32x4 o[2];
; #pragma unroll
;                 for (int n = 0; n < 2; ++n) { const f32x4 a = acc[ai][0][m][n] * r, b = acc[ai][1][m][n] * r;
;                     o[n] = (f32x4){silu_f(a[0]) * b[0], silu_f(a[1]) * b[1], silu_f(a[2]) * b[2], silu_f(a[3]) * b[3]}; }
;                 if (F8OUT) { u32x2 w; w.x = pack4_fp8(o[0]); w.y = pack4_fp8(o[1]); *(u32x2*)((unsigned char*)h + (size_t)(row0 + ai * HALF + m * 16) * FFN + col0) = w; }
;                 else *(u32x4*)(h + (size_t)(row0 + ai * HALF + m * 16) * FFN + col0) = pack8(o[0], o[1]);
	v_pk_mul_f32 v[6:7], v[80:81], v[6:7]
	v_pk_mul_f32 v[8:9], v[70:71], v[8:9]
	v_pk_mul_f32 v[10:11], v[72:73], v[10:11]
	v_pk_mul_f32 v[4:5], v[74:75], v[4:5]
	v_pk_mul_f32 v[6:7], v[76:77], v[6:7]
	v_pk_mul_f32 v[8:9], v[66:67], v[8:9]
	v_pk_mul_f32 v[10:11], v[68:69], v[10:11]
	v_pk_mul_f32 v[4:5], v[4:5], v[24:25] op_sel_hi:[1,0]
	v_pk_mul_f32 v[6:7], v[6:7], v[24:25] op_sel_hi:[1,0]
	v_pk_mul_f32 v[8:9], v[8:9], v[24:25] op_sel_hi:[1,0]
	v_pk_mul_f32 v[10:11], v[10:11], v[24:25] op_sel_hi:[1,0]
	v_med3_f32 v4, v4, s64, v250
	v_med3_f32 v5, v5, s64, v250
	v_med3_f32 v6, v6, s64, v250
	v_med3_f32 v7, v7, s64, v250
	v_med3_f32 v8, v8, s64, v250
	v_med3_f32 v9, v9, s64, v250
	v_med3_f32 v10, v10, s64, v250
	v_med3_f32 v11, v11, s64, v250
	v_cvt_pk_fp8_f32 v14, v4, v5
	v_cvt_pk_fp8_f32 v15, v8, v9
	s_nop 0
	v_cvt_pk_fp8_f32 v14, v6, v7 op_sel:[0,0,1]
	v_cvt_pk_fp8_f32 v15, v10, v11 op_sel:[0,0,1]
	s_nop 1
	v_permlane16_swap_b32_e32 v12, v14
	v_permlane16_swap_b32_e32 v13, v15
	v_add_u32_e32 v18, 0x80, v0
	v_mad_i64_i32 v[18:19], s[22:23], v18, s73, v[2:3]
	global_store_dwordx4 v[18:19], v[12:15], off
	v_pk_mul_f32 v[4:5], v[62:63], v[22:23] op_sel_hi:[1,0]
	v_pk_mul_f32 v[6:7], v[64:65], v[22:23] op_sel_hi:[1,0]
	v_pk_mul_f32 v[8:9], v[54:55], v[22:23] op_sel_hi:[1,0]
	v_pk_mul_f32 v[10:11], v[56:57], v[22:23] op_sel_hi:[1,0]
	v_exp_f32_e32 v4, v4
	v_exp_f32_e32 v5, v5
	v_exp_f32_e32 v6, v6
	v_exp_f32_e32 v7, v7
	v_exp_f32_e32 v8, v8
	v_exp_f32_e32 v9, v9
	v_exp_f32_e32 v10, v10
	v_exp_f32_e32 v11, v11
	v_pk_add_f32 v[4:5], v[4:5], v[26:27] op_sel_hi:[1,0]
	v_pk_add_f32 v[6:7], v[6:7], v[26:27] op_sel_hi:[1,0]
	v_pk_add_f32 v[8:9], v[8:9], v[26:27] op_sel_hi:[1,0]
	v_pk_add_f32 v[10:11], v[10:11], v[26:27] op_sel_hi:[1,0]
	v_rcp_f32_e32 v4, v4
	v_rcp_f32_e32 v5, v5
	v_rcp_f32_e32 v6, v6
	v_rcp_f32_e32 v7, v7
	v_rcp_f32_e32 v8, v8
	v_rcp_f32_e32 v9, v9
	v_rcp_f32_e32 v10, v10
	v_rcp_f32_e32 v11, v11
	v_pk_mul_f32 v[4:5], v[62:63], v[4:5]
	v_pk_mul_f32 v[6:7], v[64:65], v[6:7]
	v_pk_mul_f32 v[8:9], v[54:55], v[8:9]
	v_pk_mul_f32 v[10:11], v[56:57], v[10:11]
	v_pk_mul_f32 v[4:5], v[58:59], v[4:5]
	v_pk_mul_f32 v[6:7], v[60:61], v[6:7]
	v_pk_mul_f32 v[8:9], v[50:51], v[8:9]
	v_pk_mul_f32 v[10:11], v[52:53], v[10:11]
	v_pk_mul_f32 v[4:5], v[4:5], v[24:25] op_sel_hi:[1,0]
	v_pk_mul_f32 v[6:7], v[6:7], v[24:25] op_sel_hi:[1,0]
	v_pk_mul_f32 v[8:9], v[8:9], v[24:25] op_sel_hi:[1,0]
	v_pk_mul_f32 v[10:11], v[10:11], v[24:25] op_sel_hi:[1,0]
	v_med3_f32 v4, v4, s64, v250
	v_med3_f32 v5, v5, s64, v250
	v_med3_f32 v6, v6, s64, v250
	v_med3_f32 v7, v7, s64, v250
	v_med3_f32 v8, v8, s64, v250
	v_med3_f32 v9, v9, s64, v250
	v_med3_f32 v10, v10, s64, v250
	v_med3_f32 v11, v11, s64, v250
	v_cvt_pk_fp8_f32 v12, v4, v5
	v_cvt_pk_fp8_f32 v13, v8, v9
	s_nop 0
	v_cvt_pk_fp8_f32 v12, v6, v7 op_sel:[0,0,1]
	v_cvt_pk_fp8_f32 v13, v10, v11 op_sel:[0,0,1]
	v_pk_mul_f32 v[4:5], v[46:47], v[22:23] op_sel_hi:[1,0]
	v_pk_mul_f32 v[6:7], v[48:49], v[22:23] op_sel_hi:[1,0]
	v_pk_mul_f32 v[8:9], v[38:39], v[22:23] op_sel_hi:[1,0]
	v_pk_mul_f32 v[10:11], v[40:41], v[22:23] op_sel_hi:[1,0]
	v_exp_f32_e32 v4, v4
	v_exp_f32_e32 v5, v5
	v_exp_f32_e32 v6, v6
	v_exp_f32_e32 v7, v7
	v_exp_f32_e32 v8, v8
	v_exp_f32_e32 v9, v9
	v_exp_f32_e32 v10, v10
	v_exp_f32_e32 v11, v11
	v_pk_add_f32 v[4:5], v[4:5], v[26:27] op_sel_hi:[1,0]
	v_pk_add_f32 v[6:7], v[6:7], v[26:27] op_sel_hi:[1,0]
	v_pk_add_f32 v[8:9], v[8:9], v[26:27] op_sel_hi:[1,0]
	v_pk_add_f32 v[10:11], v[10:11], v[26:27] op_sel_hi:[1,0]
	v_rcp_f32_e32 v4, v4
	v_rcp_f32_e32 v5, v5
	v_rcp_f32_e32 v6, v6
	v_rcp_f32_e32 v7, v7
	v_rcp_f32_e32 v8, v8
	v_rcp_f32_e32 v9, v9
	v_rcp_f32_e32 v10, v10
	v_rcp_f32_e32 v11, v11
	v_pk_mul_f32 v[4:5], v[46:47], v[4:5]
	v_pk_mul_f32 v[6:7], v[48:49], v[6:7]
	v_pk_mul_f32 v[8:9], v[38:39], v[8:9]
	v_pk_mul_f32 v[10:11], v[40:41], v[10:11]
	v_pk_mul_f32 v[4:5], v[42:43], v[4:5]
	v_pk_mul_f32 v[6:7], v[44:45], v[6:7]
	v_pk_mul_f32 v[8:9], v[34:35], v[8:9]
	v_pk_mul_f32 v[10:11], v[36:37], v[10:11]
	v_pk_mul_f32 v[4:5], v[4:5], v[24:25] op_sel_hi:[1,0]
	v_pk_mul_f32 v[6:7], v[6:7], v[24:25] op_sel_hi:[1,0]
	v_pk_mul_f32 v[8:9], v[8:9], v[24:25] op_sel_hi:[1,0]
	v_pk_mul_f32 v[10:11], v[10:11], v[24:25] op_sel_hi:[1,0]
	v_med3_f32 v4, v4, s64, v250
	v_med3_f32 v5, v5, s64, v250
	v_med3_f32 v6, v6, s64, v250
	v_med3_f32 v7, v7, s64, v250
	v_med3_f32 v8, v8, s64, v250
	v_med3_f32 v9, v9, s64, v250
	v_med3_f32 v10, v10, s64, v250
	v_med3_f32 v11, v11, s64, v250
	v_cvt_pk_fp8_f32 v14, v4, v5
	v_cvt_pk_fp8_f32 v15, v8, v9
	s_nop 0
	v_cvt_pk_fp8_f32 v14, v6, v7 op_sel:[0,0,1]
	v_cvt_pk_fp8_f32 v15, v10, v11 op_sel:[0,0,1]
	s_nop 1
	v_permlane16_swap_b32_e32 v12, v14
	v_permlane16_swap_b32_e32 v13, v15
	v_add_u32_e32 v18, 0xa0, v0
	v_mad_i64_i32 v[18:19], s[22:23], v18, s73, v[2:3]
	s_mov_b64 s[22:23], -1
	s_and_b64 vcc, exec, s[2:3]
	global_store_dwordx4 v[18:19], v[12:15], off
	s_cbranch_vccnz .LBB0_1358
	s_andn2_b64 vcc, exec, s[14:15]
	s_cbranch_vccnz .LBB0_1357
	s_barrier
	s_branch .LBB0_1357
